# baseline (speedup 1.0000x reference)
.LBB1_12:
	s_mov_b32 s0, s44
	s_add_i32 s44, s44, 1
	s_cmp_ge_u32 s44, s42
	s_cselect_b64 s[22:23], -1, 0
	s_cmp_lt_u32 s44, s42
	s_cselect_b32 s2, s44, s0
	s_waitcnt vmcnt(0)
	s_lshl_b32 s0, s2, 4
	s_mov_b32 s1, s17
	s_mov_b32 m0, s43
	ds_read_b128 v[76:79], v119 offset:32768
	ds_read_b128 v[80:83], v119 offset:36864
	ds_read_b128 v[84:87], v120 offset:32768
	ds_read_b128 v[88:91], v120 offset:36864
	ds_read_b128 v[92:95], v121
	ds_read_b128 v[96:99], v121 offset:4096
	ds_read_b128 v[128:131], v122
	ds_read_b128 v[132:135], v122 offset:4096
	ds_read_b128 v[72:75], v123
	s_waitcnt lgkmcnt(0)
	v_lshl_add_u64 v[70:71], s[0:1], 2, v[2:3]
	global_load_lds_dword v[70:71], off
	ds_read_b128 v[156:159], v115
	ds_read_b128 v[160:163], v115 offset:1024
	ds_read_b128 v[164:167], v115 offset:2048
	v_cvt_pk_bf16_f32 v136, v76, v77
	v_cvt_pk_bf16_f32 v137, v78, v79
	v_cvt_pk_bf16_f32 v138, v84, v85
	v_cvt_pk_bf16_f32 v139, v86, v87
	v_cvt_pk_bf16_f32 v140, v92, v93
	v_cvt_pk_bf16_f32 v141, v94, v95
	v_cvt_pk_bf16_f32 v142, v128, v129
	v_cvt_pk_bf16_f32 v143, v130, v131
	v_cvt_pk_bf16_f32 v144, v80, v81
	v_cvt_pk_bf16_f32 v145, v82, v83
	v_cvt_pk_bf16_f32 v146, v88, v89
	v_cvt_pk_bf16_f32 v147, v90, v91
	v_cvt_pk_bf16_f32 v128, v96, v97
	v_cvt_pk_bf16_f32 v129, v98, v99
	v_cvt_pk_bf16_f32 v130, v132, v133
	v_cvt_pk_bf16_f32 v131, v134, v135
	s_lshl_b32 s0, s2, 13
	s_cmp_lt_u32 s44, s42
	s_cselect_b32 s0, s0, 0x1e848000
	s_mov_b32 s61, s0
	s_add_i32 s63, s44, 1
	s_cmp_eq_u32 s63, s42
	s_cselect_b32 s63, 1, 0
	s_cmp_gt_u32 s60, 20
	s_cselect_b32 s63, s63, 0
	ds_read_b128 v[132:135], v115 offset:3072
	s_waitcnt lgkmcnt(3)
	v_mfma_f32_16x16x32_bf16 v[148:151], v[136:139], v[156:159], v[36:39]
	ds_read_b128 v[156:159], v115 offset:4096
	s_waitcnt lgkmcnt(3)
	v_mfma_f32_16x16x32_bf16 v[152:155], v[136:139], v[160:163], v[40:43]
	ds_read_b128 v[160:163], v115 offset:5120
	s_waitcnt lgkmcnt(3)
	v_mfma_f32_16x16x32_bf16 v[96:99], v[136:139], v[164:167], v[44:47]
	ds_read_b128 v[164:167], v115 offset:6144
	s_waitcnt lgkmcnt(3)
	v_mfma_f32_16x16x32_bf16 v[92:95], v[136:139], v[132:135], v[48:51]
	ds_read_b128 v[132:135], v115 offset:7168
	s_waitcnt lgkmcnt(3)
	v_mfma_f32_16x16x32_bf16 v[88:91], v[136:139], v[156:159], v[52:55]
	ds_read_b128 v[156:159], v115 offset:8192
	s_waitcnt lgkmcnt(3)
	v_mfma_f32_16x16x32_bf16 v[84:87], v[136:139], v[160:163], v[56:59]
	ds_read_b128 v[160:163], v115 offset:9216
	s_waitcnt lgkmcnt(3)
	v_mfma_f32_16x16x32_bf16 v[80:83], v[136:139], v[164:167], v[60:63]
	ds_read_b128 v[164:167], v115 offset:10240
	s_waitcnt lgkmcnt(3)
	v_mfma_f32_16x16x32_bf16 v[76:79], v[136:139], v[132:135], v[64:67]
	ds_read_b128 v[132:135], v115 offset:11264
	s_waitcnt lgkmcnt(3)
	v_mfma_f32_16x16x32_bf16 v[148:151], v[140:143], v[156:159], v[148:151]
	ds_read_b128 v[156:159], v115 offset:12288
	s_waitcnt lgkmcnt(3)
	v_mfma_f32_16x16x32_bf16 v[152:155], v[140:143], v[160:163], v[152:155]
	ds_read_b128 v[160:163], v115 offset:13312
	s_waitcnt lgkmcnt(3)
	v_mfma_f32_16x16x32_bf16 v[96:99], v[140:143], v[164:167], v[96:99]
	ds_read_b128 v[164:167], v115 offset:14336
	s_waitcnt lgkmcnt(3)
	v_mfma_f32_16x16x32_bf16 v[92:95], v[140:143], v[132:135], v[92:95]
	ds_read_b128 v[132:135], v115 offset:15360
	s_waitcnt lgkmcnt(3)
	v_mfma_f32_16x16x32_bf16 v[88:91], v[140:143], v[156:159], v[88:91]
	ds_read_b128 v[156:159], v115 offset:16384
	s_waitcnt lgkmcnt(3)
	v_mfma_f32_16x16x32_bf16 v[84:87], v[140:143], v[160:163], v[84:87]
	ds_read_b128 v[160:163], v115 offset:17408
	s_waitcnt lgkmcnt(3)
	v_mfma_f32_16x16x32_bf16 v[80:83], v[140:143], v[164:167], v[80:83]
	ds_read_b128 v[164:167], v115 offset:18432
	s_waitcnt lgkmcnt(3)
	v_mfma_f32_16x16x32_bf16 v[76:79], v[140:143], v[132:135], v[76:79]
	ds_read_b128 v[132:135], v115 offset:19456
	s_waitcnt lgkmcnt(3)
	s_mov_b32 m0, s47
	s_nop 0
	buffer_load_dwordx4 v113, s[12:15], s61 offen nt lds
	s_cmp_eq_u32 s63, 0
	s_cbranch_scc1 .Lmain_noburst
	s_or_b32 s62, s61, 0x800
	s_mov_b32 m0, s48
	s_nop 0
	buffer_load_dwordx4 v113, s[12:15], s62 offen nt lds
	s_or_b32 s62, s61, 0x1000
	s_mov_b32 m0, s49
	s_nop 0
	buffer_load_dwordx4 v113, s[12:15], s62 offen nt lds
	s_or_b32 s62, s61, 0x1800
	s_mov_b32 m0, s50
	s_nop 0
	buffer_load_dwordx4 v113, s[12:15], s62 offen nt lds
	s_or_b32 s62, s61, 0x100
	s_mov_b32 m0, s51
	s_nop 0
	buffer_load_dwordx4 v113, s[12:15], s62 offen nt lds
	s_or_b32 s62, s61, 0x900
	s_mov_b32 m0, s52
	s_nop 0
	buffer_load_dwordx4 v113, s[12:15], s62 offen nt lds
	s_or_b32 s62, s61, 0x1100
	s_mov_b32 m0, s53
	s_nop 0
	buffer_load_dwordx4 v113, s[12:15], s62 offen nt lds
	s_or_b32 s62, s61, 0x1900
	s_mov_b32 m0, s54
	s_nop 0
	buffer_load_dwordx4 v113, s[12:15], s62 offen nt lds
